# cache policy: read-once f32 master-weight loads of the bf16 conversion loops marked non-temporal (nt)
# speedup vs baseline: 1.0020x; 1.0020x over previous
.LBB0_163:
	s_andn2_b64 vcc, exec, s[14:15]
	s_cbranch_vccnz .LBB0_165
	s_and_b32 s1, s20, 0xffc0
	s_add_i32 s14, s1, 0xffff3700
	s_and_b32 s1, s19, 0x300
	v_add_u32_e32 v2, s14, v34
	v_add_u32_e32 v4, s14, v40
	v_add_u32_e32 v10, s14, v42
	v_add_u32_e32 v12, s14, v44
	v_add_u32_e32 v18, s14, v46
	v_add_u32_e32 v20, s14, v48
	s_lshl_b32 s80, s1, 2
	v_ashrrev_i32_e32 v3, 31, v2
	v_ashrrev_i32_e32 v5, 31, v4
	v_ashrrev_i32_e32 v11, 31, v10
	v_ashrrev_i32_e32 v13, 31, v12
	v_ashrrev_i32_e32 v19, 31, v18
	v_ashrrev_i32_e32 v21, 31, v20
	v_lshl_add_u64 v[30:31], v[94:95], 0, s[80:81]
	v_lshlrev_b64 v[2:3], 12, v[2:3]
	v_lshlrev_b64 v[4:5], 12, v[4:5]
	v_lshlrev_b64 v[10:11], 12, v[10:11]
	v_lshlrev_b64 v[12:13], 12, v[12:13]
	v_lshlrev_b64 v[18:19], 12, v[18:19]
	v_lshlrev_b64 v[20:21], 12, v[20:21]
	v_lshl_add_u64 v[2:3], v[30:31], 0, v[2:3]
	v_lshl_add_u64 v[6:7], v[30:31], 0, v[4:5]
	v_lshl_add_u64 v[10:11], v[30:31], 0, v[10:11]
	v_lshl_add_u64 v[14:15], v[30:31], 0, v[12:13]
	v_lshl_add_u64 v[18:19], v[30:31], 0, v[18:19]
	v_lshl_add_u64 v[22:23], v[30:31], 0, v[20:21]
	global_load_dwordx4 v[2:5], v[2:3], off nt
	s_nop 0
	global_load_dwordx4 v[6:9], v[6:7], off nt
	s_nop 0
	global_load_dwordx4 v[10:13], v[10:11], off nt
	s_nop 0
	global_load_dwordx4 v[14:17], v[14:15], off nt
	s_nop 0
	global_load_dwordx4 v[18:21], v[18:19], off nt
	s_nop 0
	global_load_dwordx4 v[22:25], v[22:23], off nt
	v_add_u32_e32 v26, s14, v50
	v_ashrrev_i32_e32 v27, 31, v26
	v_lshlrev_b64 v[26:27], 12, v[26:27]
	v_add_u32_e32 v32, s14, v52
	v_lshl_add_u64 v[26:27], v[30:31], 0, v[26:27]
	v_ashrrev_i32_e32 v33, 31, v32
	global_load_dwordx4 v[26:29], v[26:27], off nt
	v_lshlrev_b64 v[32:33], 12, v[32:33]
	v_lshl_add_u64 v[30:31], v[30:31], 0, v[32:33]
	global_load_dwordx4 v[30:33], v[30:31], off nt
	v_add_u32_e32 v39, v108, v109
	v_add_u32_e32 v41, v108, v110
	v_add_u32_e32 v43, v108, v111
	v_add_u32_e32 v45, v108, v112
	v_add_u32_e32 v47, v108, v113
	v_add_u32_e32 v49, v108, v116
	v_add_u32_e32 v51, v108, v117
	v_add_u32_e32 v53, v108, v118
	s_mov_b32 s15, s81
	v_add_u32_e32 v98, s1, v119
	s_lshl_b64 s[14:15], s[14:15], 1
	v_readlane_b32 s16, v251, 63
	v_ashrrev_i32_e32 v99, 31, v98
	s_add_u32 s14, s16, s14
	v_readlane_b32 s16, v252, 0
	v_lshlrev_b64 v[98:99], 11, v[98:99]
	s_addc_u32 s15, s16, s15
	v_lshlrev_b32_e32 v114, 1, v64
	s_waitcnt vmcnt(7)
	ds_write2_b32 v39, v2, v3 offset1:1
	ds_write2_b32 v39, v4, v5 offset0:2 offset1:3
	s_waitcnt vmcnt(6)
	ds_write2_b32 v41, v6, v7 offset1:1
	ds_write2_b32 v41, v8, v9 offset0:2 offset1:3
	s_waitcnt vmcnt(5)
	ds_write2_b32 v43, v10, v11 offset1:1
	ds_write2_b32 v43, v12, v13 offset0:2 offset1:3
	s_waitcnt vmcnt(4)
	ds_write2_b32 v45, v14, v15 offset1:1
	ds_write2_b32 v45, v16, v17 offset0:2 offset1:3
	s_waitcnt vmcnt(3)
	ds_write2_b32 v47, v18, v19 offset1:1
	ds_write2_b32 v47, v20, v21 offset0:2 offset1:3
	s_waitcnt vmcnt(2)
	ds_write2_b32 v49, v22, v23 offset1:1
	ds_write2_b32 v49, v24, v25 offset0:2 offset1:3
	s_waitcnt vmcnt(1)
	ds_write2_b32 v51, v26, v27 offset1:1
	ds_write2_b32 v51, v28, v29 offset0:2 offset1:3
	s_waitcnt vmcnt(0)
	ds_write2_b32 v53, v30, v31 offset1:1
	ds_write2_b32 v53, v32, v33 offset0:2 offset1:3
	s_waitcnt lgkmcnt(0)
	s_barrier
	ds_read_b32 v2, v120
	ds_read_b32 v3, v120 offset:1044
	ds_read_b32 v4, v120 offset:2088
	ds_read_b32 v5, v120 offset:3132
	ds_read_b32 v8, v120 offset:4176
	ds_read_b32 v9, v120 offset:5220
	ds_read_b32 v10, v120 offset:6264
	ds_read_b32 v11, v120 offset:7308
	v_lshl_add_u64 v[6:7], s[14:15], 0, v[98:99]
	s_waitcnt lgkmcnt(6)
	v_cvt_pk_bf16_f32 v2, v2, v3
	s_waitcnt lgkmcnt(4)
	v_cvt_pk_bf16_f32 v3, v4, v5
	s_waitcnt lgkmcnt(2)
	v_cvt_pk_bf16_f32 v4, v8, v9
	s_waitcnt lgkmcnt(0)
	v_cvt_pk_bf16_f32 v5, v10, v11
	v_lshl_add_u64 v[6:7], v[6:7], 0, v[114:115]
	global_store_dwordx4 v[6:7], v[2:5], off
	ds_read_b32 v2, v122
	ds_read_b32 v3, v122 offset:1044
	ds_read_b32 v4, v122 offset:2088
	ds_read_b32 v5, v122 offset:3132
	ds_read_b32 v7, v122 offset:4176
	ds_read_b32 v8, v122 offset:5220
	ds_read_b32 v9, v122 offset:6264
	ds_read_b32 v10, v122 offset:7308
	v_add_u32_e32 v6, s1, v121
	s_waitcnt lgkmcnt(6)
	v_cvt_pk_bf16_f32 v2, v2, v3
	s_waitcnt lgkmcnt(4)
	v_cvt_pk_bf16_f32 v3, v4, v5
	s_waitcnt lgkmcnt(2)
	v_cvt_pk_bf16_f32 v4, v7, v8
	v_ashrrev_i32_e32 v7, 31, v6
	v_lshlrev_b64 v[6:7], 11, v[6:7]
	v_lshl_add_u64 v[6:7], s[14:15], 0, v[6:7]
	s_waitcnt lgkmcnt(0)
	v_cvt_pk_bf16_f32 v5, v9, v10
	v_lshl_add_u64 v[6:7], v[6:7], 0, v[114:115]
	global_store_dwordx4 v[6:7], v[2:5], off
	ds_read_b32 v2, v124
	ds_read_b32 v3, v124 offset:1044
	ds_read_b32 v4, v124 offset:2088
	ds_read_b32 v5, v124 offset:3132
	ds_read_b32 v7, v124 offset:4176
	ds_read_b32 v8, v124 offset:5220
	ds_read_b32 v9, v124 offset:6264
	ds_read_b32 v10, v124 offset:7308
	v_add_u32_e32 v6, s1, v123
	s_waitcnt lgkmcnt(6)
	v_cvt_pk_bf16_f32 v2, v2, v3
	s_waitcnt lgkmcnt(4)
	v_cvt_pk_bf16_f32 v3, v4, v5
	s_waitcnt lgkmcnt(2)
	v_cvt_pk_bf16_f32 v4, v7, v8
	v_ashrrev_i32_e32 v7, 31, v6
	v_lshlrev_b64 v[6:7], 11, v[6:7]
	v_lshl_add_u64 v[6:7], s[14:15], 0, v[6:7]
	s_waitcnt lgkmcnt(0)
	v_cvt_pk_bf16_f32 v5, v9, v10
	v_lshl_add_u64 v[6:7], v[6:7], 0, v[114:115]
	global_store_dwordx4 v[6:7], v[2:5], off
	ds_read_b32 v2, v126
	ds_read_b32 v3, v126 offset:1044
	ds_read_b32 v4, v126 offset:2088
	ds_read_b32 v5, v126 offset:3132
	ds_read_b32 v7, v126 offset:4176
	ds_read_b32 v8, v126 offset:5220
	ds_read_b32 v9, v126 offset:6264
	ds_read_b32 v10, v126 offset:7308
	v_add_u32_e32 v6, s1, v125
	s_waitcnt lgkmcnt(6)
	v_cvt_pk_bf16_f32 v2, v2, v3
	s_waitcnt lgkmcnt(4)
	v_cvt_pk_bf16_f32 v3, v4, v5
	s_waitcnt lgkmcnt(2)
	v_cvt_pk_bf16_f32 v4, v7, v8
	v_ashrrev_i32_e32 v7, 31, v6
	v_lshlrev_b64 v[6:7], 11, v[6:7]
	v_lshl_add_u64 v[6:7], s[14:15], 0, v[6:7]
	s_waitcnt lgkmcnt(0)
	v_cvt_pk_bf16_f32 v5, v9, v10
	v_lshl_add_u64 v[6:7], v[6:7], 0, v[114:115]
	global_store_dwordx4 v[6:7], v[2:5], off
	s_barrier

.LBB0_166:
	s_andn2_b64 vcc, exec, s[14:15]
	s_cbranch_vccnz .LBB0_184
	s_and_b32 s1, s23, 0xff
	s_mul_i32 s1, s1, 57
	s_lshr_b32 s1, s1, 9
	s_mul_i32 s14, s1, 9
	s_sub_i32 s14, s23, s14
	s_and_b32 s14, s14, 0xff
	s_lshl_b32 s16, s1, 6
	s_lshl_b32 s1, s14, 8
	v_or_b32_e32 v2, s1, v38
	s_movk_i32 s15, 0x860
	s_lshl_b32 s80, s14, 10
	v_cmp_gt_u32_e32 vcc, s15, v2
	v_lshl_add_u64 v[98:99], v[96:97], 0, s[80:81]
	v_mov_b32_e32 v2, 0
	v_mov_b32_e32 v6, 0
	v_mov_b32_e32 v7, 0
	v_mov_b32_e32 v8, 0
	v_mov_b32_e32 v9, 0
	s_and_saveexec_b64 s[14:15], vcc
	s_cbranch_execz .LBB0_169
	v_add_u32_e32 v3, s16, v34
	s_movk_i32 s17, 0x2180
	v_mad_i64_i32 v[4:5], s[24:25], v3, s17, v[98:99]
	global_load_dwordx4 v[6:9], v[4:5], off nt
.LBB0_169:
	s_or_b64 exec, exec, s[14:15]
	v_mov_b32_e32 v3, 0
	v_mov_b32_e32 v4, 0
	v_mov_b32_e32 v5, 0
	s_and_saveexec_b64 s[14:15], vcc
	s_cbranch_execz .LBB0_171
	v_add_u32_e32 v2, s16, v40
	s_movk_i32 s17, 0x2180
	v_mad_i64_i32 v[2:3], s[24:25], v2, s17, v[98:99]
	global_load_dwordx4 v[2:5], v[2:3], off nt
.LBB0_171:
	s_or_b64 exec, exec, s[14:15]
	v_mov_b32_e32 v10, 0
	v_mov_b32_e32 v14, 0
	v_mov_b32_e32 v15, 0
	v_mov_b32_e32 v16, 0
	v_mov_b32_e32 v17, 0
	s_and_saveexec_b64 s[14:15], vcc
	s_cbranch_execz .LBB0_173
	v_add_u32_e32 v11, s16, v42
	s_movk_i32 s17, 0x2180
	v_mad_i64_i32 v[12:13], s[24:25], v11, s17, v[98:99]
	global_load_dwordx4 v[14:17], v[12:13], off nt
.LBB0_173:
	s_or_b64 exec, exec, s[14:15]
	v_mov_b32_e32 v11, 0
	v_mov_b32_e32 v12, 0
	v_mov_b32_e32 v13, 0
	s_and_saveexec_b64 s[14:15], vcc
	s_cbranch_execz .LBB0_175
	v_add_u32_e32 v10, s16, v44
	s_movk_i32 s17, 0x2180
	v_mad_i64_i32 v[10:11], s[24:25], v10, s17, v[98:99]
	global_load_dwordx4 v[10:13], v[10:11], off nt
.LBB0_175:
	s_or_b64 exec, exec, s[14:15]
	v_mov_b32_e32 v18, 0
	v_mov_b32_e32 v22, 0
	v_mov_b32_e32 v23, 0
	v_mov_b32_e32 v24, 0
	v_mov_b32_e32 v25, 0
	s_and_saveexec_b64 s[14:15], vcc
	s_cbranch_execz .LBB0_177
	v_add_u32_e32 v19, s16, v46
	s_movk_i32 s17, 0x2180
	v_mad_i64_i32 v[20:21], s[24:25], v19, s17, v[98:99]
	global_load_dwordx4 v[22:25], v[20:21], off nt
.LBB0_177:
	s_or_b64 exec, exec, s[14:15]
	v_mov_b32_e32 v19, 0
	v_mov_b32_e32 v20, 0
	v_mov_b32_e32 v21, 0
	s_and_saveexec_b64 s[14:15], vcc
	s_cbranch_execz .LBB0_179
	v_add_u32_e32 v18, s16, v48
	s_movk_i32 s17, 0x2180
	v_mad_i64_i32 v[18:19], s[24:25], v18, s17, v[98:99]
	global_load_dwordx4 v[18:21], v[18:19], off nt
.LBB0_179:
	s_or_b64 exec, exec, s[14:15]
	v_mov_b32_e32 v26, 0
	v_mov_b32_e32 v30, 0
	v_mov_b32_e32 v31, 0
	v_mov_b32_e32 v32, 0
	v_mov_b32_e32 v33, 0
	s_and_saveexec_b64 s[14:15], vcc
	s_cbranch_execz .LBB0_181
	v_add_u32_e32 v27, s16, v50
	s_movk_i32 s17, 0x2180
	v_mad_i64_i32 v[28:29], s[24:25], v27, s17, v[98:99]
	global_load_dwordx4 v[30:33], v[28:29], off nt
.LBB0_181:
	s_or_b64 exec, exec, s[14:15]
	v_mov_b32_e32 v27, 0
	v_mov_b32_e32 v28, 0
	v_mov_b32_e32 v29, 0
	s_and_saveexec_b64 s[14:15], vcc
	s_cbranch_execz .LBB0_183
	v_add_u32_e32 v26, s16, v52
	s_movk_i32 s17, 0x2180
	v_mad_i64_i32 v[26:27], s[24:25], v26, s17, v[98:99]
	global_load_dwordx4 v[26:29], v[26:27], off nt

.LBB0_185:
	s_andn2_b64 vcc, exec, s[14:15]
	s_cbranch_vccnz .LBB0_187
	s_add_i32 s1, s23, 0xfffff800
	s_lshr_b32 s80, s1, 5
	s_lshl_b64 s[14:15], s[80:81], 21
	s_add_u32 s16, s70, s14
	s_addc_u32 s17, s71, s15
	s_and_b32 s24, s20, 0x1c0
	s_and_b32 s1, s19, 0x300
	s_lshl_b64 s[14:15], s[80:81], 20
	v_readlane_b32 s25, v252, 3
	s_add_u32 s25, s25, s14
	v_readlane_b32 s14, v252, 4
	s_addc_u32 s26, s14, s15
	s_lshl_b32 s14, s1, 2
	s_add_u32 s14, s16, s14
	v_add_u32_e32 v2, s24, v34
	v_add_u32_e32 v4, s24, v40
	v_add_u32_e32 v10, s24, v42
	v_add_u32_e32 v12, s24, v44
	v_add_u32_e32 v18, s24, v46
	v_add_u32_e32 v20, s24, v48
	s_addc_u32 s15, s17, 0
	v_lshlrev_b32_e32 v114, 2, v38
	v_ashrrev_i32_e32 v3, 31, v2
	v_ashrrev_i32_e32 v5, 31, v4
	v_ashrrev_i32_e32 v11, 31, v10
	v_ashrrev_i32_e32 v13, 31, v12
	v_ashrrev_i32_e32 v19, 31, v18
	v_ashrrev_i32_e32 v21, 31, v20
	v_lshl_add_u64 v[30:31], s[14:15], 0, v[114:115]
	v_lshlrev_b64 v[2:3], 12, v[2:3]
	v_lshlrev_b64 v[4:5], 12, v[4:5]
	v_lshlrev_b64 v[10:11], 12, v[10:11]
	v_lshlrev_b64 v[12:13], 12, v[12:13]
	v_lshlrev_b64 v[18:19], 12, v[18:19]
	v_lshlrev_b64 v[20:21], 12, v[20:21]
	v_lshl_add_u64 v[2:3], v[30:31], 0, v[2:3]
	v_lshl_add_u64 v[6:7], v[30:31], 0, v[4:5]
	v_lshl_add_u64 v[10:11], v[30:31], 0, v[10:11]
	v_lshl_add_u64 v[14:15], v[30:31], 0, v[12:13]
	v_lshl_add_u64 v[18:19], v[30:31], 0, v[18:19]
	v_lshl_add_u64 v[22:23], v[30:31], 0, v[20:21]
	global_load_dwordx4 v[2:5], v[2:3], off nt
	s_nop 0
	global_load_dwordx4 v[6:9], v[6:7], off nt
	s_nop 0
	global_load_dwordx4 v[10:13], v[10:11], off nt
	s_nop 0
	global_load_dwordx4 v[14:17], v[14:15], off nt
	s_nop 0
	global_load_dwordx4 v[18:21], v[18:19], off nt
	s_nop 0
	global_load_dwordx4 v[22:25], v[22:23], off nt
	v_add_u32_e32 v26, s24, v50
	v_ashrrev_i32_e32 v27, 31, v26
	v_lshlrev_b64 v[26:27], 12, v[26:27]
	v_add_u32_e32 v32, s24, v52
	v_lshl_add_u64 v[26:27], v[30:31], 0, v[26:27]
	v_ashrrev_i32_e32 v33, 31, v32
	global_load_dwordx4 v[26:29], v[26:27], off nt
	v_lshlrev_b64 v[32:33], 12, v[32:33]
	v_lshl_add_u64 v[30:31], v[30:31], 0, v[32:33]
	global_load_dwordx4 v[30:33], v[30:31], off nt
	v_add_u32_e32 v39, v108, v109
	v_add_u32_e32 v41, v108, v110
	v_add_u32_e32 v43, v108, v111
	v_add_u32_e32 v45, v108, v112
	v_add_u32_e32 v47, v108, v113
	v_add_u32_e32 v49, v108, v116
	v_add_u32_e32 v51, v108, v117
	v_add_u32_e32 v53, v108, v118
	v_add_u32_e32 v98, s1, v119
	s_lshl_b32 s14, s24, 1
	s_add_u32 s14, s25, s14
	v_ashrrev_i32_e32 v99, 31, v98
	s_addc_u32 s15, s26, 0
	v_lshlrev_b32_e32 v114, 1, v64
	s_waitcnt vmcnt(7)
	ds_write2_b32 v39, v2, v3 offset1:1
	ds_write2_b32 v39, v4, v5 offset0:2 offset1:3
	s_waitcnt vmcnt(6)
	ds_write2_b32 v41, v6, v7 offset1:1
	ds_write2_b32 v41, v8, v9 offset0:2 offset1:3
	s_waitcnt vmcnt(5)
	ds_write2_b32 v43, v10, v11 offset1:1
	ds_write2_b32 v43, v12, v13 offset0:2 offset1:3
	s_waitcnt vmcnt(4)
	ds_write2_b32 v45, v14, v15 offset1:1
	ds_write2_b32 v45, v16, v17 offset0:2 offset1:3
	s_waitcnt vmcnt(3)
	ds_write2_b32 v47, v18, v19 offset1:1
	ds_write2_b32 v47, v20, v21 offset0:2 offset1:3
	s_waitcnt vmcnt(2)
	ds_write2_b32 v49, v22, v23 offset1:1
	ds_write2_b32 v49, v24, v25 offset0:2 offset1:3
	s_waitcnt vmcnt(1)
	ds_write2_b32 v51, v26, v27 offset1:1
	ds_write2_b32 v51, v28, v29 offset0:2 offset1:3
	s_waitcnt vmcnt(0)
	ds_write2_b32 v53, v30, v31 offset1:1
	ds_write2_b32 v53, v32, v33 offset0:2 offset1:3
	s_waitcnt lgkmcnt(0)
	s_barrier
	ds_read_b32 v2, v120
	ds_read_b32 v3, v120 offset:1044
	ds_read_b32 v4, v120 offset:2088
	ds_read_b32 v5, v120 offset:3132
	ds_read_b32 v6, v120 offset:4176
	ds_read_b32 v7, v120 offset:5220
	ds_read_b32 v8, v120 offset:6264
	ds_read_b32 v9, v120 offset:7308
	s_waitcnt lgkmcnt(6)
	v_cvt_pk_bf16_f32 v2, v2, v3
	s_waitcnt lgkmcnt(4)
	v_cvt_pk_bf16_f32 v3, v4, v5
	s_waitcnt lgkmcnt(2)
	v_cvt_pk_bf16_f32 v4, v6, v7
	v_lshlrev_b64 v[6:7], 10, v[98:99]
	v_lshl_add_u64 v[6:7], s[14:15], 0, v[6:7]
	s_waitcnt lgkmcnt(0)
	v_cvt_pk_bf16_f32 v5, v8, v9
	v_lshl_add_u64 v[6:7], v[6:7], 0, v[114:115]
	global_store_dwordx4 v[6:7], v[2:5], off
	ds_read_b32 v2, v122
	ds_read_b32 v3, v122 offset:1044
	ds_read_b32 v4, v122 offset:2088
	ds_read_b32 v5, v122 offset:3132
	ds_read_b32 v7, v122 offset:4176
	ds_read_b32 v8, v122 offset:5220
	ds_read_b32 v9, v122 offset:6264
	ds_read_b32 v10, v122 offset:7308
	v_add_u32_e32 v6, s1, v121
	s_waitcnt lgkmcnt(6)
	v_cvt_pk_bf16_f32 v2, v2, v3
	s_waitcnt lgkmcnt(4)
	v_cvt_pk_bf16_f32 v3, v4, v5
	s_waitcnt lgkmcnt(2)
	v_cvt_pk_bf16_f32 v4, v7, v8
	v_ashrrev_i32_e32 v7, 31, v6
	v_lshlrev_b64 v[6:7], 10, v[6:7]
	v_lshl_add_u64 v[6:7], s[14:15], 0, v[6:7]
	s_waitcnt lgkmcnt(0)
	v_cvt_pk_bf16_f32 v5, v9, v10
	v_lshl_add_u64 v[6:7], v[6:7], 0, v[114:115]
	global_store_dwordx4 v[6:7], v[2:5], off
	ds_read_b32 v2, v124
	ds_read_b32 v3, v124 offset:1044
	ds_read_b32 v4, v124 offset:2088
	ds_read_b32 v5, v124 offset:3132
	ds_read_b32 v7, v124 offset:4176
	ds_read_b32 v8, v124 offset:5220
	ds_read_b32 v9, v124 offset:6264
	ds_read_b32 v10, v124 offset:7308
	v_add_u32_e32 v6, s1, v123
	s_waitcnt lgkmcnt(6)
	v_cvt_pk_bf16_f32 v2, v2, v3
	s_waitcnt lgkmcnt(4)
	v_cvt_pk_bf16_f32 v3, v4, v5
	s_waitcnt lgkmcnt(2)
	v_cvt_pk_bf16_f32 v4, v7, v8
	v_ashrrev_i32_e32 v7, 31, v6
	v_lshlrev_b64 v[6:7], 10, v[6:7]
	v_lshl_add_u64 v[6:7], s[14:15], 0, v[6:7]
	s_waitcnt lgkmcnt(0)
	v_cvt_pk_bf16_f32 v5, v9, v10
	v_lshl_add_u64 v[6:7], v[6:7], 0, v[114:115]
	global_store_dwordx4 v[6:7], v[2:5], off
	ds_read_b32 v2, v126
	ds_read_b32 v3, v126 offset:1044
	ds_read_b32 v4, v126 offset:2088
	ds_read_b32 v5, v126 offset:3132
	ds_read_b32 v7, v126 offset:4176
	ds_read_b32 v8, v126 offset:5220
	ds_read_b32 v9, v126 offset:6264
	ds_read_b32 v10, v126 offset:7308
	v_add_u32_e32 v6, s1, v125
	s_waitcnt lgkmcnt(6)
	v_cvt_pk_bf16_f32 v2, v2, v3
	s_waitcnt lgkmcnt(4)
	v_cvt_pk_bf16_f32 v3, v4, v5
	s_waitcnt lgkmcnt(2)
	v_cvt_pk_bf16_f32 v4, v7, v8
	v_ashrrev_i32_e32 v7, 31, v6
	v_lshlrev_b64 v[6:7], 10, v[6:7]
	v_lshl_add_u64 v[6:7], s[14:15], 0, v[6:7]
	s_waitcnt lgkmcnt(0)
	v_cvt_pk_bf16_f32 v5, v9, v10
	v_lshl_add_u64 v[6:7], v[6:7], 0, v[114:115]
	global_store_dwordx4 v[6:7], v[2:5], off
	s_barrier

.LBB0_188:
	s_andn2_b64 vcc, exec, s[14:15]
	s_cbranch_vccnz .LBB0_149
	s_ashr_i32 s1, s23, 31
	s_lshr_b32 s1, s1, 22
	s_add_i32 s1, s23, s1
	s_ashr_i32 s17, s1, 10
	s_and_b32 s1, s1, 0xfc00
	s_sub_i32 s1, s23, s1
	s_sext_i32_i16 s14, s1
	s_bfe_u32 s14, s14, 0x5001a
	s_add_i32 s15, s1, s14
	s_sext_i32_i16 s14, s15
	s_and_b32 s15, s15, 0xffe0
	s_sub_i32 s15, s1, s15
	s_bfe_u32 s16, s15, 0x10007
	s_add_i32 s15, s15, s16
	s_bfe_i32 s15, s15, 0x80000
	s_sext_i32_i16 s16, s15
	s_bfe_u32 s15, s1, 0x1000f
	s_add_i32 s15, s1, s15
	s_and_b32 s15, s15, 0xfffe
	s_lshr_b32 s14, s14, 5
	s_sub_i32 s1, s1, s15
	s_add_i32 s15, s23, 0x3ff
	s_cmpk_lt_u32 s15, 0x7ff
	s_cselect_b32 s26, s67, s69
	s_cselect_b32 s27, s66, s68
	s_bfe_i64 s[14:15], s[14:15], 0x100000
	s_lshl_b64 s[24:25], s[14:15], 21
	s_add_u32 s27, s27, s24
	s_sext_i32_i16 s1, s1
	s_addc_u32 s26, s26, s25
	s_lshl_b32 s14, s16, 5
	s_and_b32 s16, s14, 0xffffffc0
	s_lshl_b32 s14, s1, 8
	v_readlane_b32 s1, v252, 5
	s_add_u32 s1, s1, s24
	v_readlane_b32 s15, v252, 6
	s_addc_u32 s28, s15, s25
	s_ashr_i32 s15, s14, 31
	s_lshl_b64 s[24:25], s[14:15], 2
	s_add_u32 s24, s27, s24
	v_add_u32_e32 v2, s16, v34
	v_add_u32_e32 v4, s16, v40
	v_add_u32_e32 v10, s16, v42
	v_add_u32_e32 v12, s16, v44
	v_add_u32_e32 v18, s16, v46
	v_add_u32_e32 v20, s16, v48
	s_addc_u32 s25, s26, s25
	v_lshlrev_b32_e32 v114, 2, v38
	v_ashrrev_i32_e32 v3, 31, v2
	v_ashrrev_i32_e32 v5, 31, v4
	v_ashrrev_i32_e32 v11, 31, v10
	v_ashrrev_i32_e32 v13, 31, v12
	v_ashrrev_i32_e32 v19, 31, v18
	v_ashrrev_i32_e32 v21, 31, v20
	v_lshl_add_u64 v[30:31], s[24:25], 0, v[114:115]
	v_lshlrev_b64 v[2:3], 11, v[2:3]
	v_lshlrev_b64 v[4:5], 11, v[4:5]
	v_lshlrev_b64 v[10:11], 11, v[10:11]
	v_lshlrev_b64 v[12:13], 11, v[12:13]
	v_lshlrev_b64 v[18:19], 11, v[18:19]
	v_lshlrev_b64 v[20:21], 11, v[20:21]
	v_lshl_add_u64 v[2:3], v[30:31], 0, v[2:3]
	v_lshl_add_u64 v[6:7], v[30:31], 0, v[4:5]
	v_lshl_add_u64 v[10:11], v[30:31], 0, v[10:11]
	v_lshl_add_u64 v[14:15], v[30:31], 0, v[12:13]
	v_lshl_add_u64 v[18:19], v[30:31], 0, v[18:19]
	v_lshl_add_u64 v[22:23], v[30:31], 0, v[20:21]
	global_load_dwordx4 v[2:5], v[2:3], off nt
	s_nop 0
	global_load_dwordx4 v[6:9], v[6:7], off nt
	s_nop 0
	global_load_dwordx4 v[10:13], v[10:11], off nt
	s_nop 0
	global_load_dwordx4 v[14:17], v[14:15], off nt
	s_nop 0
	global_load_dwordx4 v[18:21], v[18:19], off nt
	s_nop 0
	global_load_dwordx4 v[22:25], v[22:23], off nt
	v_add_u32_e32 v26, s16, v50
	v_ashrrev_i32_e32 v27, 31, v26
	v_lshlrev_b64 v[26:27], 11, v[26:27]
	v_add_u32_e32 v32, s16, v52
	v_lshl_add_u64 v[26:27], v[30:31], 0, v[26:27]
	v_ashrrev_i32_e32 v33, 31, v32
	global_load_dwordx4 v[26:29], v[26:27], off nt
	v_lshlrev_b64 v[32:33], 11, v[32:33]
	v_lshl_add_u64 v[30:31], v[30:31], 0, v[32:33]
	global_load_dwordx4 v[30:33], v[30:31], off nt
	v_add_u32_e32 v39, v108, v109
	v_add_co_u32_e64 v59, vcc, s17, 1
	v_add_u32_e32 v41, v108, v110
	v_add_u32_e32 v43, v108, v111
	v_add_u32_e32 v45, v108, v112
	v_add_u32_e32 v47, v108, v113
	v_add_u32_e32 v49, v108, v116
	v_add_u32_e32 v51, v108, v117
	v_add_u32_e32 v53, v108, v118
	v_add_u32_e32 v55, s14, v119
	s_ashr_i32 s17, s16, 31
	s_lshl_b64 s[16:17], s[16:17], 1
	s_add_u32 s16, s1, s16
	s_addc_u32 s17, s28, s17
	v_lshlrev_b32_e32 v114, 1, v64
	s_waitcnt vmcnt(7)
	ds_write2_b32 v39, v2, v3 offset1:1
	ds_write2_b32 v39, v4, v5 offset0:2 offset1:3
	s_waitcnt vmcnt(6)
	ds_write2_b32 v41, v6, v7 offset1:1
	ds_write2_b32 v41, v8, v9 offset0:2 offset1:3
	s_waitcnt vmcnt(5)
	ds_write2_b32 v43, v10, v11 offset1:1
	ds_write2_b32 v43, v12, v13 offset0:2 offset1:3
	s_waitcnt vmcnt(4)
	ds_write2_b32 v45, v14, v15 offset1:1
	ds_write2_b32 v45, v16, v17 offset0:2 offset1:3
	s_waitcnt vmcnt(3)
	ds_write2_b32 v47, v18, v19 offset1:1
	ds_write2_b32 v47, v20, v21 offset0:2 offset1:3
	s_waitcnt vmcnt(2)
	ds_write2_b32 v49, v22, v23 offset1:1
	ds_write2_b32 v49, v24, v25 offset0:2 offset1:3
	s_waitcnt vmcnt(1)
	ds_write2_b32 v51, v26, v27 offset1:1
	ds_write2_b32 v51, v28, v29 offset0:2 offset1:3
	s_waitcnt vmcnt(0)
	ds_write2_b32 v53, v30, v31 offset1:1
	ds_write2_b32 v53, v32, v33 offset0:2 offset1:3
	v_lshlrev_b32_e32 v2, 7, v59
	v_add_u32_e32 v8, 0xffffff80, v2
	v_lshlrev_b32_e32 v6, 1, v55
	s_waitcnt lgkmcnt(0)
	s_barrier
	ds_read_b32 v2, v120
	ds_read_b32 v3, v120 offset:1044
	ds_read_b32 v4, v120 offset:2088
	ds_read_b32 v5, v120 offset:3132
	ds_read_b32 v7, v120 offset:4176
	ds_read_b32 v9, v120 offset:5220
	ds_read_b32 v10, v120 offset:6264
	ds_read_b32 v11, v120 offset:7308
	v_and_b32_e32 v6, 0xffffff00, v6
	v_or_b32_e32 v12, v8, v127
	v_add_u32_e32 v6, v12, v6
	v_cndmask_b32_e32 v6, v6, v55, vcc
	s_waitcnt lgkmcnt(6)
	v_cvt_pk_bf16_f32 v2, v2, v3
	s_waitcnt lgkmcnt(4)
	v_cvt_pk_bf16_f32 v3, v4, v5
	s_waitcnt lgkmcnt(2)
	v_cvt_pk_bf16_f32 v4, v7, v9
	v_ashrrev_i32_e32 v7, 31, v6
	v_lshlrev_b64 v[6:7], 11, v[6:7]
	v_lshl_add_u64 v[6:7], s[16:17], 0, v[6:7]
	s_waitcnt lgkmcnt(0)
	v_cvt_pk_bf16_f32 v5, v10, v11
	v_lshl_add_u64 v[6:7], v[6:7], 0, v[114:115]
	global_store_dwordx4 v[6:7], v[2:5], off
	v_add_u32_e32 v6, s14, v121
	v_lshlrev_b32_e32 v12, 1, v6
	ds_read_b32 v2, v122
	ds_read_b32 v3, v122 offset:1044
	ds_read_b32 v4, v122 offset:2088
	ds_read_b32 v5, v122 offset:3132
	ds_read_b32 v7, v122 offset:4176
	ds_read_b32 v9, v122 offset:5220
	ds_read_b32 v10, v122 offset:6264
	ds_read_b32 v11, v122 offset:7308
	v_and_b32_e32 v12, 0xffffff00, v12
	v_or_b32_e32 v13, v8, v128
	v_add_u32_e32 v12, v13, v12
	v_cndmask_b32_e32 v6, v12, v6, vcc
	s_waitcnt lgkmcnt(6)
	v_cvt_pk_bf16_f32 v2, v2, v3
	s_waitcnt lgkmcnt(4)
	v_cvt_pk_bf16_f32 v3, v4, v5
	s_waitcnt lgkmcnt(2)
	v_cvt_pk_bf16_f32 v4, v7, v9
	v_ashrrev_i32_e32 v7, 31, v6
	v_lshlrev_b64 v[6:7], 11, v[6:7]
	v_lshl_add_u64 v[6:7], s[16:17], 0, v[6:7]
	s_waitcnt lgkmcnt(0)
	v_cvt_pk_bf16_f32 v5, v10, v11
	v_lshl_add_u64 v[6:7], v[6:7], 0, v[114:115]
	global_store_dwordx4 v[6:7], v[2:5], off
	v_add_u32_e32 v6, s14, v123
	v_lshlrev_b32_e32 v12, 1, v6
	ds_read_b32 v2, v124
	ds_read_b32 v3, v124 offset:1044
	ds_read_b32 v4, v124 offset:2088
	ds_read_b32 v5, v124 offset:3132
	ds_read_b32 v7, v124 offset:4176
	ds_read_b32 v9, v124 offset:5220
	ds_read_b32 v10, v124 offset:6264
	ds_read_b32 v11, v124 offset:7308
	v_and_b32_e32 v12, 0xffffff00, v12
	v_or_b32_e32 v13, v8, v129
	v_add_u32_e32 v12, v13, v12
	v_cndmask_b32_e32 v6, v12, v6, vcc
	s_waitcnt lgkmcnt(6)
	v_cvt_pk_bf16_f32 v2, v2, v3
	s_waitcnt lgkmcnt(4)
	v_cvt_pk_bf16_f32 v3, v4, v5
	s_waitcnt lgkmcnt(2)
	v_cvt_pk_bf16_f32 v4, v7, v9
	v_ashrrev_i32_e32 v7, 31, v6
	v_lshlrev_b64 v[6:7], 11, v[6:7]
	v_lshl_add_u64 v[6:7], s[16:17], 0, v[6:7]
	s_waitcnt lgkmcnt(0)
	v_cvt_pk_bf16_f32 v5, v10, v11
	v_lshl_add_u64 v[6:7], v[6:7], 0, v[114:115]
	global_store_dwordx4 v[6:7], v[2:5], off
	v_add_u32_e32 v6, s14, v125
	v_lshlrev_b32_e32 v12, 1, v6
	ds_read_b32 v2, v126
	ds_read_b32 v3, v126 offset:1044
	ds_read_b32 v4, v126 offset:2088
	ds_read_b32 v5, v126 offset:3132
	ds_read_b32 v7, v126 offset:4176
	ds_read_b32 v9, v126 offset:5220
	ds_read_b32 v10, v126 offset:6264
	ds_read_b32 v11, v126 offset:7308
	v_and_b32_e32 v12, 0xffffff00, v12
	v_or_b32_e32 v8, v8, v130
	v_add_u32_e32 v8, v8, v12
	v_cndmask_b32_e32 v6, v8, v6, vcc
	s_waitcnt lgkmcnt(6)
	v_cvt_pk_bf16_f32 v2, v2, v3
	s_waitcnt lgkmcnt(4)
	v_cvt_pk_bf16_f32 v3, v4, v5
	s_waitcnt lgkmcnt(2)
	v_cvt_pk_bf16_f32 v4, v7, v9
	v_ashrrev_i32_e32 v7, 31, v6
	v_lshlrev_b64 v[6:7], 11, v[6:7]
	v_lshl_add_u64 v[6:7], s[16:17], 0, v[6:7]
	s_waitcnt lgkmcnt(0)
	v_cvt_pk_bf16_f32 v5, v10, v11
	v_lshl_add_u64 v[6:7], v[6:7], 0, v[114:115]
	global_store_dwordx4 v[6:7], v[2:5], off
	s_barrier
	s_branch .LBB0_149

.LBB0_949:
	s_cmp_lg_u64 s[26:27], 0
	v_lshlrev_b32_e32 v1, 4, v67
	s_cselect_b64 s[30:31], -1, 0
	s_cmp_eq_u64 s[26:27], 0
	s_waitcnt vmcnt(0)
	v_and_b32_e32 v30, 0x70, v1
	s_cbranch_scc1 .LBB0_955
	v_ashrrev_i32_e32 v1, 3, v67
	v_ashrrev_i32_e32 v2, 31, v1
	v_mul_lo_u32 v4, s28, v2
	v_mul_lo_u32 v5, s29, v1
	v_mad_u64_u32 v[2:3], s[0:1], s28, v1, 0
	v_add_u32_e32 v1, 64, v67
	v_ashrrev_i32_e32 v1, 3, v1
	v_add3_u32 v3, v3, v4, v5
	v_ashrrev_i32_e32 v4, 31, v1
	v_mul_lo_u32 v6, s28, v4
	v_mul_lo_u32 v7, s29, v1
	v_mad_u64_u32 v[4:5], s[0:1], s28, v1, 0
	v_add3_u32 v5, v5, v6, v7
	v_lshl_add_u64 v[2:3], v[2:3], 2, s[26:27]
	v_mov_b32_e32 v31, v115
	v_lshl_add_u64 v[4:5], v[4:5], 2, s[26:27]
	v_lshl_add_u64 v[2:3], v[2:3], 0, v[30:31]
	v_lshl_add_u64 v[6:7], v[4:5], 0, v[30:31]
	global_load_dwordx4 v[2:5], v[2:3], off nt
	s_nop 0
	global_load_dwordx4 v[6:9], v[6:7], off nt
	v_cndmask_b32_e64 v1, 0, 1, s[30:31]
	v_cmp_ne_u32_e64 s[0:1], 1, v1
	s_andn2_b64 vcc, exec, s[30:31]
	s_cbranch_vccnz .LBB0_956
.LBB0_951:
	v_add_u32_e32 v1, 0x80, v67
	v_ashrrev_i32_e32 v1, 3, v1
	v_ashrrev_i32_e32 v10, 31, v1
	v_mul_lo_u32 v12, s28, v10
	v_mul_lo_u32 v13, s29, v1
	v_mad_u64_u32 v[10:11], s[30:31], s28, v1, 0
	v_add_u32_e32 v1, 0xc0, v67
	v_ashrrev_i32_e32 v1, 3, v1
	v_add3_u32 v11, v11, v12, v13
	v_ashrrev_i32_e32 v12, 31, v1
	v_mul_lo_u32 v14, s28, v12
	v_mul_lo_u32 v15, s29, v1
	v_mad_u64_u32 v[12:13], s[30:31], s28, v1, 0
	v_add3_u32 v13, v13, v14, v15
	v_lshl_add_u64 v[10:11], v[10:11], 2, s[26:27]
	v_mov_b32_e32 v31, v115
	v_lshl_add_u64 v[12:13], v[12:13], 2, s[26:27]
	v_lshl_add_u64 v[10:11], v[10:11], 0, v[30:31]
	v_lshl_add_u64 v[14:15], v[12:13], 0, v[30:31]
	global_load_dwordx4 v[10:13], v[10:11], off nt
	s_nop 0
	global_load_dwordx4 v[14:17], v[14:15], off nt
	s_and_b64 vcc, exec, s[0:1]
	s_cbranch_vccnz .LBB0_957
.LBB0_952:
	v_add_u32_e32 v1, 0x100, v67
	v_ashrrev_i32_e32 v1, 3, v1
	v_ashrrev_i32_e32 v18, 31, v1
	v_mul_lo_u32 v20, s28, v18
	v_mul_lo_u32 v21, s29, v1
	v_mad_u64_u32 v[18:19], s[30:31], s28, v1, 0
	v_add_u32_e32 v1, 0x140, v67
	v_ashrrev_i32_e32 v1, 3, v1
	v_add3_u32 v19, v19, v20, v21
	v_ashrrev_i32_e32 v20, 31, v1
	v_mul_lo_u32 v22, s28, v20
	v_mul_lo_u32 v23, s29, v1
	v_mad_u64_u32 v[20:21], s[30:31], s28, v1, 0
	v_add3_u32 v21, v21, v22, v23
	v_lshl_add_u64 v[18:19], v[18:19], 2, s[26:27]
	v_mov_b32_e32 v31, v115
	v_lshl_add_u64 v[20:21], v[20:21], 2, s[26:27]
	v_lshl_add_u64 v[18:19], v[18:19], 0, v[30:31]
	v_lshl_add_u64 v[22:23], v[20:21], 0, v[30:31]
	global_load_dwordx4 v[18:21], v[18:19], off nt
	s_nop 0
	global_load_dwordx4 v[22:25], v[22:23], off nt
	s_and_b64 vcc, exec, s[0:1]
	s_cbranch_vccnz .LBB0_958
.LBB0_953:
	v_add_u32_e32 v1, 0x180, v67
	v_ashrrev_i32_e32 v1, 3, v1
	v_ashrrev_i32_e32 v26, 31, v1
	v_mul_lo_u32 v28, s28, v26
	v_mul_lo_u32 v29, s29, v1
	v_mad_u64_u32 v[26:27], s[0:1], s28, v1, 0
	v_add_u32_e32 v1, 0x1c0, v67
	v_ashrrev_i32_e32 v1, 3, v1
	v_ashrrev_i32_e32 v32, 31, v1
	v_mul_lo_u32 v34, s28, v32
	v_mul_lo_u32 v35, s29, v1
	v_mad_u64_u32 v[32:33], s[0:1], s28, v1, 0
	v_add3_u32 v27, v27, v28, v29
	v_add3_u32 v33, v33, v34, v35
	v_lshl_add_u64 v[26:27], v[26:27], 2, s[26:27]
	v_mov_b32_e32 v31, v115
	v_lshl_add_u64 v[32:33], v[32:33], 2, s[26:27]
	v_lshl_add_u64 v[26:27], v[26:27], 0, v[30:31]
	v_lshl_add_u64 v[30:31], v[32:33], 0, v[30:31]
	global_load_dwordx4 v[26:29], v[26:27], off nt
	s_nop 0
	global_load_dwordx4 v[30:33], v[30:31], off nt
	s_andn2_b64 vcc, exec, s[24:25]
	s_cbranch_vccz .LBB0_959
	s_branch .LBB0_995

.LBB0_960:
	v_mul_lo_u32 v27, s39, v48
	v_mul_lo_u32 v30, s38, v51
	v_mad_u64_u32 v[28:29], s[0:1], s38, v48, 0
	v_add3_u32 v29, v29, v30, v27
	v_mul_lo_u32 v32, s39, v50
	v_mul_lo_u32 v33, s38, v53
	v_mad_u64_u32 v[30:31], s[0:1], s38, v50, 0
	v_add3_u32 v31, v31, v33, v32
	v_lshl_add_u64 v[28:29], v[28:29], 2, s[34:35]
	v_mov_b32_e32 v27, v115
	v_lshl_add_u64 v[30:31], v[30:31], 2, s[34:35]
	v_lshl_add_u64 v[28:29], v[28:29], 0, v[26:27]
	v_lshl_add_u64 v[30:31], v[30:31], 0, v[26:27]
	global_load_dwordx4 v[26:29], v[28:29], off nt
	s_nop 0
	global_load_dwordx4 v[30:33], v[30:31], off nt

.LBB0_986:
	s_cmp_lg_u64 s[34:35], 0
	s_cselect_b64 s[40:41], -1, 0
	s_cmp_eq_u64 s[34:35], 0
	v_lshlrev_b32_e32 v26, 2, v34
	s_cbranch_scc1 .LBB0_990
	v_mul_lo_u32 v4, s39, v36
	v_mul_lo_u32 v5, s38, v1
	v_mad_u64_u32 v[2:3], s[0:1], s38, v36, 0
	v_add3_u32 v3, v3, v5, v4
	v_mul_lo_u32 v6, s39, v38
	v_mul_lo_u32 v7, s38, v41
	v_mad_u64_u32 v[4:5], s[0:1], s38, v38, 0
	v_add3_u32 v5, v5, v7, v6
	v_lshl_add_u64 v[2:3], v[2:3], 2, s[34:35]
	v_mov_b32_e32 v27, v115
	v_lshl_add_u64 v[4:5], v[4:5], 2, s[34:35]
	v_lshl_add_u64 v[2:3], v[2:3], 0, v[26:27]
	v_lshl_add_u64 v[6:7], v[4:5], 0, v[26:27]
	global_load_dwordx4 v[2:5], v[2:3], off nt
	s_nop 0
	global_load_dwordx4 v[6:9], v[6:7], off nt
	v_cndmask_b32_e64 v10, 0, 1, s[40:41]
	v_cmp_ne_u32_e64 s[0:1], 1, v10
	s_andn2_b64 vcc, exec, s[40:41]
	s_cbranch_vccnz .LBB0_991
.LBB0_988:
	v_mul_lo_u32 v12, s39, v40
	v_mul_lo_u32 v13, s38, v43
	v_mad_u64_u32 v[10:11], s[40:41], s38, v40, 0
	v_add3_u32 v11, v11, v13, v12
	v_mul_lo_u32 v14, s39, v42
	v_mul_lo_u32 v15, s38, v45
	v_mad_u64_u32 v[12:13], s[40:41], s38, v42, 0
	v_add3_u32 v13, v13, v15, v14
	v_lshl_add_u64 v[10:11], v[10:11], 2, s[34:35]
	v_mov_b32_e32 v27, v115
	v_lshl_add_u64 v[12:13], v[12:13], 2, s[34:35]
	v_lshl_add_u64 v[10:11], v[10:11], 0, v[26:27]
	v_lshl_add_u64 v[14:15], v[12:13], 0, v[26:27]
	global_load_dwordx4 v[10:13], v[10:11], off nt
	s_nop 0
	global_load_dwordx4 v[14:17], v[14:15], off nt
	s_and_b64 vcc, exec, s[0:1]
	s_cbranch_vccnz .LBB0_992
.LBB0_989:
	v_mul_lo_u32 v20, s39, v44
	v_mul_lo_u32 v21, s38, v47
	v_mad_u64_u32 v[18:19], s[40:41], s38, v44, 0
	v_add3_u32 v19, v19, v21, v20
	v_mul_lo_u32 v22, s39, v46
	v_mul_lo_u32 v23, s38, v49
	v_mad_u64_u32 v[20:21], s[40:41], s38, v46, 0
	v_add3_u32 v21, v21, v23, v22
	v_lshl_add_u64 v[18:19], v[18:19], 2, s[34:35]
	v_mov_b32_e32 v27, v115
	v_lshl_add_u64 v[20:21], v[20:21], 2, s[34:35]
	v_lshl_add_u64 v[18:19], v[18:19], 0, v[26:27]
	v_lshl_add_u64 v[22:23], v[20:21], 0, v[26:27]
	global_load_dwordx4 v[18:21], v[18:19], off nt
	s_nop 0
	global_load_dwordx4 v[22:25], v[22:23], off nt
	s_and_b64 vcc, exec, s[0:1]
	s_cbranch_vccz .LBB0_960
	s_branch .LBB0_993
